# grid barrier: each CU's L1 invalidate moved to right after its workgroup drains (it overlaps the wait for the other workgroups; nothing can refill L1 meanwhile)
# speedup vs baseline: 1.0283x; 1.0132x over previous
; __device__ __forceinline__ unsigned xb_ld(unsigned* p)              { return __hip_atomic_load(p, __ATOMIC_RELAXED, __HIP_MEMORY_SCOPE_AGENT); }
; __device__ __forceinline__ unsigned xb_add(unsigned* p, unsigned v) { return __hip_atomic_fetch_add(p, v, __ATOMIC_RELAXED, __HIP_MEMORY_SCOPE_AGENT); }
; __device__ __forceinline__ bool xb_tid0(unsigned w0) { return w0 != 0u && __builtin_amdgcn_mbcnt_hi(0xffffffffu, __builtin_amdgcn_mbcnt_lo(0xffffffffu, 0u)) == 0u; }
; __device__ __forceinline__ void xcd_barrier_complete(unsigned* bar, unsigned x, unsigned& nloc, unsigned& nx) {
;     const unsigned G = gridDim.x * gridDim.y * gridDim.z;
;     unsigned sum, cnt, mine, sp = 0u;
;     for (;;) {
;         sum = 0u; cnt = 0u; mine = 0u;
; #pragma unroll
;         for (unsigned j = 0; j < 16; ++j) { const unsigned c = xb_ld(&bar[XB_XCNT(j)]); sum += c; cnt += (c > 0u) ? 1u : 0u; mine = (j == x) ? c : mine; }
; __device__ __forceinline__ void xcd_barrier(const XcdBarrier& b) {
;     asm volatile("s_waitcnt vmcnt(0)" ::: "memory");
;     __syncthreads();
;     if (xb_tid0(b.w0)) {
;         unsigned* bar = b.bar;
;         __builtin_amdgcn_s_waitcnt(0);
;         unsigned nloc = b.st[0], nx = b.st[1];
;         if (nloc == 0u) { xcd_barrier_complete(bar, b.x, nloc, nx); b.st[0] = nloc; b.st[1] = nx; }
;         const unsigned old = xb_add(&bar[XB_XSUB(b.x)], 1u);
.LBB0_97:
	s_cmp_lt_i32 s95, 2
	s_cbranch_scc1 .LBB0_153
	s_waitcnt vmcnt(0)
	s_andn2_b64 vcc, exec, s[96:97]
	s_barrier
	s_cbranch_vccnz .LBB0_152
	v_cmp_eq_u32_e32 vcc, 0, v75
	s_and_saveexec_b64 s[4:5], vcc
	s_cbranch_execz .LBB0_151
	s_add_i32 s1, 0, 0x23020
	v_mov_b32_e32 v0, s1
	s_waitcnt vmcnt(0) expcnt(0) lgkmcnt(0)
	buffer_inv sc1
	ds_read_b32 v2, v0
	s_add_i32 s1, 0, 0x23024
	v_mov_b32_e32 v0, s1
	ds_read_b32 v0, v0
	s_waitcnt lgkmcnt(1)
	v_cmp_ne_u32_e32 vcc, 0, v2
	s_cbranch_vccnz .LBB0_115
	v_readlane_b32 s6, v252, 0
	v_readlane_b32 s7, v252, 1
	s_load_dwordx2 s[2:3], s[6:7], 0x4
	s_add_u32 s6, s92, 0x4200
	s_addc_u32 s7, s93, 0
	s_add_u32 s8, s92, 0x4400
	s_addc_u32 s9, s93, 0
	s_add_u32 s12, s92, 0x4500
	s_addc_u32 s13, s93, 0
	s_add_u32 s14, s92, 0x4600
	s_addc_u32 s15, s93, 0
	s_add_u32 s16, s92, 0x4700
	s_addc_u32 s17, s93, 0
	s_add_u32 s18, s92, 0x4800
	s_addc_u32 s19, s93, 0
	s_add_u32 s20, s92, 0x4900
	s_addc_u32 s21, s93, 0
	s_add_u32 s22, s92, 0x4a00
	s_addc_u32 s23, s93, 0
	s_add_u32 s24, s92, 0x4b00
	s_addc_u32 s25, s93, 0
	s_add_u32 s26, s92, 0x4c00
	s_addc_u32 s27, s93, 0
	s_add_u32 s28, s92, 0x4d00
	s_addc_u32 s29, s93, 0
	s_add_u32 s30, s92, 0x4e00
	s_addc_u32 s31, s93, 0
	s_add_u32 s34, s92, 0x4f00
	s_addc_u32 s35, s93, 0
	s_add_u32 s36, s92, 0x5000
	s_addc_u32 s37, s93, 0
	s_add_u32 s38, s92, 0x5100
	s_addc_u32 s39, s93, 0
	s_add_u32 s40, s92, 0x5200
	s_addc_u32 s41, s93, 0
	s_waitcnt lgkmcnt(0)
	s_mul_i32 s1, s2, s90
	s_add_u32 s42, s92, 0x5300
	s_mul_i32 s1, s1, s3
	s_addc_u32 s43, s93, 0
	s_mov_b32 s2, 1
	v_mov_b32_e32 v16, 0
	s_branch .LBB0_103

; __device__ __forceinline__ unsigned xb_ld(unsigned* p)              { return __hip_atomic_load(p, __ATOMIC_RELAXED, __HIP_MEMORY_SCOPE_AGENT); }
; #define XB_SPIN(cond, bar) do { unsigned _sp = 0; while (cond) { __builtin_amdgcn_s_sleep(1); \
;     if ((++_sp & 255u) == 0u) { if (xb_ld(&(bar)[XB_TMO])) break; if (_sp > XB_SPIN_CAP) { atomicAdd(&(bar)[XB_TMO], 1u); break; } } } } while (0)
; __device__ __forceinline__ void xcd_barrier(const XcdBarrier& b) {
;     ...
;             XB_SPIN(xb_ld(&bar[XB_XGEN(b.x)]) == gen, bar);
;             __builtin_amdgcn_fence(__ATOMIC_ACQUIRE, "agent");
;             asm volatile("s_waitcnt vmcnt(0)" ::: "memory");
.LBB0_130:
	s_or_b64 exec, exec, s[12:13]
	s_waitcnt vmcnt(0)
	s_waitcnt vmcnt(0)

; __device__ __forceinline__ unsigned xb_ld(unsigned* p)              { return __hip_atomic_load(p, __ATOMIC_RELAXED, __HIP_MEMORY_SCOPE_AGENT); }
; __device__ __forceinline__ unsigned xb_add(unsigned* p, unsigned v) { return __hip_atomic_fetch_add(p, v, __ATOMIC_RELAXED, __HIP_MEMORY_SCOPE_AGENT); }
; #define XB_SPIN(cond, bar) do { unsigned _sp = 0; while (cond) { __builtin_amdgcn_s_sleep(1); \
;     if ((++_sp & 255u) == 0u) { if (xb_ld(&(bar)[XB_TMO])) break; if (_sp > XB_SPIN_CAP) { atomicAdd(&(bar)[XB_TMO], 1u); break; } } } } while (0)
; __device__ __forceinline__ void xcd_barrier(const XcdBarrier& b) {
;     ...
;             if (og + 1u == (tg + 1u) * nx) xb_add(&bar[XB_TOPGEN], 1u);
;             else XB_SPIN(xb_ld(&bar[XB_TOPGEN]) == tg, bar);
;             __builtin_amdgcn_fence(__ATOMIC_ACQUIRE, "agent");
;             xb_add(&bar[XB_XGEN(b.x)], 1u);
;             asm volatile("s_waitcnt vmcnt(0)" ::: "memory");
.LBB0_148:
	s_or_b64 exec, exec, s[8:9]
	s_mov_b64 s[8:9], exec
	v_mbcnt_lo_u32_b32 v0, s8, 0
	v_mbcnt_hi_u32_b32 v0, s9, v0
	v_cmp_eq_u32_e32 vcc, 0, v0
	s_waitcnt vmcnt(0)
	s_and_saveexec_b64 s[12:13], vcc
	s_cbranch_execz .LBB0_150
	s_bcnt1_i32_b64 s1, s[8:9]
	v_mov_b32_e32 v0, 0x2000
	v_mov_b32_e32 v1, s1
	global_atomic_add v0, v1, s[6:7] offset:1024

; __device__ __forceinline__ unsigned xb_add(unsigned* p, unsigned v) { return __hip_atomic_fetch_add(p, v, __ATOMIC_RELAXED, __HIP_MEMORY_SCOPE_AGENT); }
; __device__ __forceinline__ bool xb_tid0(unsigned w0) { return w0 != 0u && __builtin_amdgcn_mbcnt_hi(0xffffffffu, __builtin_amdgcn_mbcnt_lo(0xffffffffu, 0u)) == 0u; }
; #define SEAM(k) do { if (IN((k) + 1)) xcd_barrier(bar); } while (0)
; __device__ __forceinline__ void xcd_barrier(const XcdBarrier& b) {
;     asm volatile("s_waitcnt vmcnt(0)" ::: "memory");
;     __syncthreads();
;     if (xb_tid0(b.w0)) {
;         unsigned* bar = b.bar;
;         __builtin_amdgcn_s_waitcnt(0);
;         unsigned nloc = b.st[0], nx = b.st[1];
;         if (nloc == 0u) { xcd_barrier_complete(bar, b.x, nloc, nx); b.st[0] = nloc; b.st[1] = nx; }
;         const unsigned old = xb_add(&bar[XB_XSUB(b.x)], 1u);
; __global__ void __launch_bounds__(512, 2) mk_fwd(Params P) {
;     ...
;             SEAM(pb + 1);
.LBB0_231:
	v_readlane_b32 s4, v254, 54
	s_add_i32 s22, s4, 2
	s_cmp_le_i32 s94, s22
	s_cselect_b64 s[4:5], -1, 0
	s_cmp_lt_i32 s22, s95
	s_cselect_b64 s[6:7], -1, 0
	s_and_b64 s[4:5], s[4:5], s[6:7]
	s_andn2_b64 vcc, exec, s[4:5]
	s_cbranch_vccnz .LBB0_287
	s_waitcnt vmcnt(0)
	s_andn2_b64 vcc, exec, s[96:97]
	s_waitcnt vmcnt(0) lgkmcnt(0)
	s_barrier
	s_cbranch_vccnz .LBB0_286
	v_cmp_eq_u32_e32 vcc, 0, v226
	s_and_saveexec_b64 s[4:5], vcc
	s_cbranch_execz .LBB0_285
	v_readlane_b32 s6, v253, 47
	s_waitcnt vmcnt(0) expcnt(0) lgkmcnt(0)
	buffer_inv sc1
	s_nop 0
	v_mov_b32_e32 v0, s6
	ds_read_b32 v2, v0
	v_readlane_b32 s6, v253, 48
	s_waitcnt lgkmcnt(0)
	v_cmp_ne_u32_e32 vcc, 0, v2
	v_mov_b32_e32 v0, s6
	ds_read_b32 v0, v0
	s_cbranch_vccnz .LBB0_249
	v_readlane_b32 s8, v252, 0
	v_readlane_b32 s9, v252, 1
	s_load_dwordx2 s[6:7], s[8:9], 0x4
	s_mov_b32 s13, 1
	s_waitcnt lgkmcnt(0)
	s_mul_i32 s12, s6, s90
	s_mul_i32 s12, s12, s7
	s_branch .LBB0_237

; __device__ __forceinline__ unsigned xb_ld(unsigned* p)              { return __hip_atomic_load(p, __ATOMIC_RELAXED, __HIP_MEMORY_SCOPE_AGENT); }
; #define XB_SPIN(cond, bar) do { unsigned _sp = 0; while (cond) { __builtin_amdgcn_s_sleep(1); \
;     if ((++_sp & 255u) == 0u) { if (xb_ld(&(bar)[XB_TMO])) break; if (_sp > XB_SPIN_CAP) { atomicAdd(&(bar)[XB_TMO], 1u); break; } } } } while (0)
; __device__ __forceinline__ void xcd_barrier(const XcdBarrier& b) {
;     ...
;             XB_SPIN(xb_ld(&bar[XB_XGEN(b.x)]) == gen, bar);
;             __builtin_amdgcn_fence(__ATOMIC_ACQUIRE, "agent");
;             asm volatile("s_waitcnt vmcnt(0)" ::: "memory");
.LBB0_264:
	s_or_b64 exec, exec, s[8:9]
	s_waitcnt vmcnt(0)
	s_waitcnt vmcnt(0)

; __device__ __forceinline__ unsigned xb_ld(unsigned* p)              { return __hip_atomic_load(p, __ATOMIC_RELAXED, __HIP_MEMORY_SCOPE_AGENT); }
; __device__ __forceinline__ unsigned xb_add(unsigned* p, unsigned v) { return __hip_atomic_fetch_add(p, v, __ATOMIC_RELAXED, __HIP_MEMORY_SCOPE_AGENT); }
; #define XB_SPIN(cond, bar) do { unsigned _sp = 0; while (cond) { __builtin_amdgcn_s_sleep(1); \
;     if ((++_sp & 255u) == 0u) { if (xb_ld(&(bar)[XB_TMO])) break; if (_sp > XB_SPIN_CAP) { atomicAdd(&(bar)[XB_TMO], 1u); break; } } } } while (0)
; __device__ __forceinline__ void xcd_barrier(const XcdBarrier& b) {
;     ...
;             if (og + 1u == (tg + 1u) * nx) xb_add(&bar[XB_TOPGEN], 1u);
;             else XB_SPIN(xb_ld(&bar[XB_TOPGEN]) == tg, bar);
;             __builtin_amdgcn_fence(__ATOMIC_ACQUIRE, "agent");
;             xb_add(&bar[XB_XGEN(b.x)], 1u);
;             asm volatile("s_waitcnt vmcnt(0)" ::: "memory");
.LBB0_282:
	s_or_b64 exec, exec, s[6:7]
	s_mov_b64 s[6:7], exec
	v_mbcnt_lo_u32_b32 v0, s6, 0
	v_mbcnt_hi_u32_b32 v0, s7, v0
	v_cmp_eq_u32_e32 vcc, 0, v0
	s_waitcnt vmcnt(0)
	s_and_saveexec_b64 s[8:9], vcc
	s_cbranch_execz .LBB0_284
	s_bcnt1_i32_b64 s6, s[6:7]
	v_mov_b32_e32 v0, s6
	v_readlane_b32 s6, v253, 7
	v_readlane_b32 s7, v253, 8
	s_nop 4
	global_atomic_add v80, v0, s[6:7]

; __device__ __forceinline__ unsigned xb_add(unsigned* p, unsigned v) { return __hip_atomic_fetch_add(p, v, __ATOMIC_RELAXED, __HIP_MEMORY_SCOPE_AGENT); }
; __device__ __forceinline__ bool xb_tid0(unsigned w0) { return w0 != 0u && __builtin_amdgcn_mbcnt_hi(0xffffffffu, __builtin_amdgcn_mbcnt_lo(0xffffffffu, 0u)) == 0u; }
; #define SEAM(k) do { if (IN((k) + 1)) xcd_barrier(bar); } while (0)
; __device__ __forceinline__ void xcd_barrier(const XcdBarrier& b) {
;     asm volatile("s_waitcnt vmcnt(0)" ::: "memory");
;     __syncthreads();
;     if (xb_tid0(b.w0)) {
;         unsigned* bar = b.bar;
;         __builtin_amdgcn_s_waitcnt(0);
;         unsigned nloc = b.st[0], nx = b.st[1];
;         if (nloc == 0u) { xcd_barrier_complete(bar, b.x, nloc, nx); b.st[0] = nloc; b.st[1] = nx; }
;         const unsigned old = xb_add(&bar[XB_XSUB(b.x)], 1u);
; __global__ void __launch_bounds__(512, 2) mk_fwd(Params P) {
;     ...
;             SEAM(pb + 2);
.LBB0_350:
	v_readlane_b32 s4, v254, 54
	s_add_i32 s22, s4, 3
	s_cmp_ge_i32 s22, s95
	s_cbranch_scc1 .LBB0_406
	s_waitcnt vmcnt(0)
	s_andn2_b64 vcc, exec, s[96:97]
	s_waitcnt lgkmcnt(0)
	s_barrier
	s_cbranch_vccnz .LBB0_405
	v_cmp_eq_u32_e32 vcc, 0, v226
	s_and_saveexec_b64 s[4:5], vcc
	s_cbranch_execz .LBB0_404
	v_readlane_b32 s6, v253, 47
	s_waitcnt vmcnt(0) expcnt(0) lgkmcnt(0)
	buffer_inv sc1
	s_nop 0
	v_mov_b32_e32 v0, s6
	ds_read_b32 v2, v0
	v_readlane_b32 s6, v253, 48
	s_waitcnt lgkmcnt(0)
	v_cmp_ne_u32_e32 vcc, 0, v2
	v_mov_b32_e32 v0, s6
	ds_read_b32 v0, v0
	s_cbranch_vccnz .LBB0_368
	v_readlane_b32 s8, v252, 0
	v_readlane_b32 s9, v252, 1
	s_load_dwordx2 s[6:7], s[8:9], 0x4
	s_mov_b32 s13, 1
	s_waitcnt lgkmcnt(0)
	s_mul_i32 s12, s6, s90
	s_mul_i32 s12, s12, s7
	s_branch .LBB0_356

; __device__ __forceinline__ unsigned xb_add(unsigned* p, unsigned v) { return __hip_atomic_fetch_add(p, v, __ATOMIC_RELAXED, __HIP_MEMORY_SCOPE_AGENT); }
; __device__ __forceinline__ bool xb_tid0(unsigned w0) { return w0 != 0u && __builtin_amdgcn_mbcnt_hi(0xffffffffu, __builtin_amdgcn_mbcnt_lo(0xffffffffu, 0u)) == 0u; }
; #define SEAM(k) do { if (IN((k) + 1)) xcd_barrier(bar); } while (0)
; __device__ __forceinline__ void xcd_barrier(const XcdBarrier& b) {
;     asm volatile("s_waitcnt vmcnt(0)" ::: "memory");
;     __syncthreads();
;     if (xb_tid0(b.w0)) {
;         unsigned* bar = b.bar;
;         __builtin_amdgcn_s_waitcnt(0);
;         unsigned nloc = b.st[0], nx = b.st[1];
;         if (nloc == 0u) { xcd_barrier_complete(bar, b.x, nloc, nx); b.st[0] = nloc; b.st[1] = nx; }
;         const unsigned old = xb_add(&bar[XB_XSUB(b.x)], 1u);
; __global__ void __launch_bounds__(512, 2) mk_fwd(Params P) {
;     ...
;             SEAM(pb + 3);
.LBB0_511:
	v_readlane_b32 s4, v254, 54
	s_add_i32 s22, s4, 4
	s_cmp_lt_i32 s22, s95
	s_cbranch_scc0 .LBB0_524
	s_waitcnt vmcnt(0)
	v_readlane_b32 s96, v254, 45
	v_readlane_b32 s97, v254, 46
	v_readlane_b32 s28, v254, 35
	s_andn2_b64 vcc, exec, s[96:97]
	s_mov_b32 s57, 0x800000
	s_mov_b32 s51, 0x5040100
	v_readlane_b32 s29, v254, 36
	s_mov_b64 s[54:55], 0x40000
	v_mov_b64_e32 v[208:209], v[198:199]
	s_waitcnt lgkmcnt(0)
	s_barrier
	s_cbranch_vccnz .LBB0_567
	v_cmp_eq_u32_e32 vcc, 0, v226
	s_and_saveexec_b64 s[4:5], vcc
	s_cbranch_execz .LBB0_566
	v_readlane_b32 s6, v253, 47
	s_waitcnt vmcnt(0) expcnt(0) lgkmcnt(0)
	buffer_inv sc1
	s_nop 0
	v_mov_b32_e32 v0, s6
	ds_read_b32 v2, v0
	v_readlane_b32 s6, v253, 48
	s_waitcnt lgkmcnt(0)
	v_cmp_ne_u32_e32 vcc, 0, v2
	v_mov_b32_e32 v0, s6
	ds_read_b32 v0, v0
	s_cbranch_vccnz .LBB0_530
	v_readlane_b32 s8, v252, 0
	v_readlane_b32 s9, v252, 1
	s_load_dwordx2 s[6:7], s[8:9], 0x4
	s_mov_b32 s13, 1
	s_waitcnt lgkmcnt(0)
	s_mul_i32 s12, s6, s90
	s_mul_i32 s12, s12, s7
	s_branch .LBB0_517

; __device__ __forceinline__ unsigned xb_add(unsigned* p, unsigned v) { return __hip_atomic_fetch_add(p, v, __ATOMIC_RELAXED, __HIP_MEMORY_SCOPE_AGENT); }
; __device__ __forceinline__ bool xb_tid0(unsigned w0) { return w0 != 0u && __builtin_amdgcn_mbcnt_hi(0xffffffffu, __builtin_amdgcn_mbcnt_lo(0xffffffffu, 0u)) == 0u; }
; #define SEAM(k) do { if (IN((k) + 1)) xcd_barrier(bar); } while (0)
; __device__ __forceinline__ void xcd_barrier(const XcdBarrier& b) {
;     asm volatile("s_waitcnt vmcnt(0)" ::: "memory");
;     __syncthreads();
;     if (xb_tid0(b.w0)) {
;         unsigned* bar = b.bar;
;         __builtin_amdgcn_s_waitcnt(0);
;         unsigned nloc = b.st[0], nx = b.st[1];
;         if (nloc == 0u) { xcd_barrier_complete(bar, b.x, nloc, nx); b.st[0] = nloc; b.st[1] = nx; }
;         const unsigned old = xb_add(&bar[XB_XSUB(b.x)], 1u);
; __global__ void __launch_bounds__(512, 2) mk_fwd(Params P) {
;     ...
;             SEAM(pb + 4);
.LBB0_574:
	v_readlane_b32 s4, v254, 54
	s_add_i32 s22, s4, 5
	s_cmp_lt_i32 s22, s95
	s_cbranch_scc0 .LBB0_630
	s_waitcnt vmcnt(0)
	s_andn2_b64 vcc, exec, s[96:97]
	s_waitcnt lgkmcnt(0)
	s_barrier
	s_cbranch_vccnz .LBB0_629
	v_cmp_eq_u32_e32 vcc, 0, v226
	s_and_saveexec_b64 s[4:5], vcc
	s_cbranch_execz .LBB0_628
	v_readlane_b32 s6, v253, 47
	s_waitcnt vmcnt(0) expcnt(0) lgkmcnt(0)
	buffer_inv sc1
	s_nop 0
	v_mov_b32_e32 v0, s6
	ds_read_b32 v2, v0
	v_readlane_b32 s6, v253, 48
	s_waitcnt lgkmcnt(0)
	v_cmp_ne_u32_e32 vcc, 0, v2
	v_mov_b32_e32 v0, s6
	ds_read_b32 v0, v0
	s_cbranch_vccnz .LBB0_592
	v_readlane_b32 s8, v252, 0
	v_readlane_b32 s9, v252, 1
	s_load_dwordx2 s[6:7], s[8:9], 0x4
	s_mov_b32 s13, 1
	s_waitcnt lgkmcnt(0)
	s_mul_i32 s12, s6, s90
	s_mul_i32 s12, s12, s7
	s_branch .LBB0_580

; __device__ __forceinline__ unsigned xb_add(unsigned* p, unsigned v) { return __hip_atomic_fetch_add(p, v, __ATOMIC_RELAXED, __HIP_MEMORY_SCOPE_AGENT); }
; __device__ __forceinline__ bool xb_tid0(unsigned w0) { return w0 != 0u && __builtin_amdgcn_mbcnt_hi(0xffffffffu, __builtin_amdgcn_mbcnt_lo(0xffffffffu, 0u)) == 0u; }
; #define SEAM(k) do { if (IN((k) + 1)) xcd_barrier(bar); } while (0)
; __device__ __forceinline__ void xcd_barrier(const XcdBarrier& b) {
;     asm volatile("s_waitcnt vmcnt(0)" ::: "memory");
;     __syncthreads();
;     if (xb_tid0(b.w0)) {
;         unsigned* bar = b.bar;
;         __builtin_amdgcn_s_waitcnt(0);
;         unsigned nloc = b.st[0], nx = b.st[1];
;         if (nloc == 0u) { xcd_barrier_complete(bar, b.x, nloc, nx); b.st[0] = nloc; b.st[1] = nx; }
;         const unsigned old = xb_add(&bar[XB_XSUB(b.x)], 1u);
; __global__ void __launch_bounds__(512, 2) mk_fwd(Params P) {
;     ...
;             SEAM(pb + 5);
.LBB0_653:
	v_readlane_b32 s4, v254, 54
	s_add_i32 s22, s4, 6
	s_cmp_ge_i32 s22, s95
	s_cbranch_scc1 .LBB0_709
	s_waitcnt vmcnt(0)
	s_andn2_b64 vcc, exec, s[96:97]
	s_waitcnt lgkmcnt(0)
	s_barrier
	s_cbranch_vccnz .LBB0_708
	v_cmp_eq_u32_e32 vcc, 0, v226
	s_and_saveexec_b64 s[4:5], vcc
	s_cbranch_execz .LBB0_707
	v_readlane_b32 s6, v253, 47
	s_waitcnt vmcnt(0) expcnt(0) lgkmcnt(0)
	buffer_inv sc1
	s_nop 0
	v_mov_b32_e32 v0, s6
	ds_read_b32 v2, v0
	v_readlane_b32 s6, v253, 48
	s_waitcnt lgkmcnt(0)
	v_cmp_ne_u32_e32 vcc, 0, v2
	v_mov_b32_e32 v0, s6
	ds_read_b32 v0, v0
	s_cbranch_vccnz .LBB0_671
	v_readlane_b32 s8, v252, 0
	v_readlane_b32 s9, v252, 1
	s_load_dwordx2 s[6:7], s[8:9], 0x4
	s_mov_b32 s13, 1
	s_waitcnt lgkmcnt(0)
	s_mul_i32 s12, s6, s90
	s_mul_i32 s12, s12, s7
	s_branch .LBB0_659

; __device__ __forceinline__ unsigned xb_add(unsigned* p, unsigned v) { return __hip_atomic_fetch_add(p, v, __ATOMIC_RELAXED, __HIP_MEMORY_SCOPE_AGENT); }
; __device__ __forceinline__ bool xb_tid0(unsigned w0) { return w0 != 0u && __builtin_amdgcn_mbcnt_hi(0xffffffffu, __builtin_amdgcn_mbcnt_lo(0xffffffffu, 0u)) == 0u; }
; #define SEAM(k) do { if (IN((k) + 1)) xcd_barrier(bar); } while (0)
; __device__ __forceinline__ void xcd_barrier(const XcdBarrier& b) {
;     asm volatile("s_waitcnt vmcnt(0)" ::: "memory");
;     __syncthreads();
;     if (xb_tid0(b.w0)) {
;         unsigned* bar = b.bar;
;         __builtin_amdgcn_s_waitcnt(0);
;         unsigned nloc = b.st[0], nx = b.st[1];
;         if (nloc == 0u) { xcd_barrier_complete(bar, b.x, nloc, nx); b.st[0] = nloc; b.st[1] = nx; }
;         const unsigned old = xb_add(&bar[XB_XSUB(b.x)], 1u);
; __global__ void __launch_bounds__(512, 2) mk_fwd(Params P) {
;     ...
;             SEAM(pb + 6);
.LBB0_719:
	v_readlane_b32 s4, v254, 54
	s_add_i32 s22, s4, 7
	s_cmp_lt_i32 s22, s95
	s_cbranch_scc0 .LBB0_775
	s_waitcnt vmcnt(0)
	s_andn2_b64 vcc, exec, s[96:97]
	s_waitcnt lgkmcnt(0)
	s_barrier
	s_cbranch_vccnz .LBB0_774
	v_cmp_eq_u32_e32 vcc, 0, v226
	s_and_saveexec_b64 s[4:5], vcc
	s_cbranch_execz .LBB0_773
	v_readlane_b32 s6, v253, 47
	s_waitcnt vmcnt(0) expcnt(0) lgkmcnt(0)
	buffer_inv sc1
	s_nop 0
	v_mov_b32_e32 v0, s6
	ds_read_b32 v2, v0
	v_readlane_b32 s6, v253, 48
	s_waitcnt lgkmcnt(0)
	v_cmp_ne_u32_e32 vcc, 0, v2
	v_mov_b32_e32 v0, s6
	ds_read_b32 v0, v0
	s_cbranch_vccnz .LBB0_737
	v_readlane_b32 s8, v252, 0
	v_readlane_b32 s9, v252, 1
	s_load_dwordx2 s[6:7], s[8:9], 0x4
	s_mov_b32 s13, 1
	s_waitcnt lgkmcnt(0)
	s_mul_i32 s12, s6, s90
	s_mul_i32 s12, s12, s7
	s_branch .LBB0_725

; __device__ __forceinline__ unsigned xb_add(unsigned* p, unsigned v) { return __hip_atomic_fetch_add(p, v, __ATOMIC_RELAXED, __HIP_MEMORY_SCOPE_AGENT); }
; __device__ __forceinline__ bool xb_tid0(unsigned w0) { return w0 != 0u && __builtin_amdgcn_mbcnt_hi(0xffffffffu, __builtin_amdgcn_mbcnt_lo(0xffffffffu, 0u)) == 0u; }
; #define SEAM(k) do { if (IN((k) + 1)) xcd_barrier(bar); } while (0)
; __device__ __forceinline__ void xcd_barrier(const XcdBarrier& b) {
;     asm volatile("s_waitcnt vmcnt(0)" ::: "memory");
;     __syncthreads();
;     if (xb_tid0(b.w0)) {
;         unsigned* bar = b.bar;
;         __builtin_amdgcn_s_waitcnt(0);
;         unsigned nloc = b.st[0], nx = b.st[1];
;         if (nloc == 0u) { xcd_barrier_complete(bar, b.x, nloc, nx); b.st[0] = nloc; b.st[1] = nx; }
;         const unsigned old = xb_add(&bar[XB_XSUB(b.x)], 1u);
; __global__ void __launch_bounds__(512, 2) mk_fwd(Params P) {
;     ...
;             SEAM(pb + 7);
.LBB0_798:
	v_readlane_b32 s4, v254, 54
	s_add_i32 s22, s4, 8
	s_cmp_ge_i32 s22, s95
	s_cbranch_scc1 .LBB0_854
	s_waitcnt vmcnt(0)
	s_andn2_b64 vcc, exec, s[96:97]
	s_waitcnt vmcnt(0) lgkmcnt(0)
	s_barrier
	s_cbranch_vccnz .LBB0_853
	v_cmp_eq_u32_e32 vcc, 0, v226
	s_and_saveexec_b64 s[4:5], vcc
	s_cbranch_execz .LBB0_852
	v_readlane_b32 s6, v253, 47
	s_waitcnt vmcnt(0) expcnt(0) lgkmcnt(0)
	buffer_inv sc1
	s_nop 0
	v_mov_b32_e32 v0, s6
	ds_read_b32 v2, v0
	v_readlane_b32 s6, v253, 48
	s_waitcnt lgkmcnt(0)
	v_cmp_ne_u32_e32 vcc, 0, v2
	v_mov_b32_e32 v0, s6
	ds_read_b32 v0, v0
	s_cbranch_vccnz .LBB0_816
	v_readlane_b32 s8, v252, 0
	v_readlane_b32 s9, v252, 1
	s_load_dwordx2 s[6:7], s[8:9], 0x4
	s_mov_b32 s13, 1
	s_waitcnt lgkmcnt(0)
	s_mul_i32 s12, s6, s90
	s_mul_i32 s12, s12, s7
	s_branch .LBB0_804

; __device__ __forceinline__ unsigned xb_add(unsigned* p, unsigned v) { return __hip_atomic_fetch_add(p, v, __ATOMIC_RELAXED, __HIP_MEMORY_SCOPE_AGENT); }
; __device__ __forceinline__ bool xb_tid0(unsigned w0) { return w0 != 0u && __builtin_amdgcn_mbcnt_hi(0xffffffffu, __builtin_amdgcn_mbcnt_lo(0xffffffffu, 0u)) == 0u; }
; #define SEAM(k) do { if (IN((k) + 1)) xcd_barrier(bar); } while (0)
; __device__ __forceinline__ void xcd_barrier(const XcdBarrier& b) {
;     asm volatile("s_waitcnt vmcnt(0)" ::: "memory");
;     __syncthreads();
;     if (xb_tid0(b.w0)) {
;         unsigned* bar = b.bar;
;         __builtin_amdgcn_s_waitcnt(0);
;         unsigned nloc = b.st[0], nx = b.st[1];
;         if (nloc == 0u) { xcd_barrier_complete(bar, b.x, nloc, nx); b.st[0] = nloc; b.st[1] = nx; }
;         const unsigned old = xb_add(&bar[XB_XSUB(b.x)], 1u);
; __global__ void __launch_bounds__(512, 2) mk_fwd(Params P) {
;     ...
;             SEAM(pb + 8);
.LBB0_914:
	v_readlane_b32 s4, v254, 54
	s_add_i32 s22, s4, 9
	s_cmp_lt_i32 s22, s95
	s_cbranch_scc0 .LBB0_927
	s_waitcnt vmcnt(0)
	v_readlane_b32 s82, v254, 30
	v_readlane_b32 s84, v254, 32
	v_readlane_b32 s28, v254, 35
	s_andn2_b64 vcc, exec, s[96:97]
	v_readlane_b32 s74, v254, 26
	v_readlane_b32 s71, v254, 28
	v_readlane_b32 s80, v254, 29
	v_readlane_b32 s83, v254, 31
	v_readlane_b32 s85, v254, 33
	s_movk_i32 s81, 0x55
	v_readlane_b32 s29, v254, 36
	s_waitcnt lgkmcnt(0)
	s_barrier
	v_readlane_b32 s75, v254, 27
	s_cbranch_vccnz .LBB0_970
	v_cmp_eq_u32_e32 vcc, 0, v226
	s_and_saveexec_b64 s[4:5], vcc
	s_cbranch_execz .LBB0_969
	v_readlane_b32 s6, v253, 47
	s_waitcnt vmcnt(0) expcnt(0) lgkmcnt(0)
	buffer_inv sc1
	s_nop 0
	v_mov_b32_e32 v0, s6
	ds_read_b32 v2, v0
	v_readlane_b32 s6, v253, 48
	s_waitcnt lgkmcnt(0)
	v_cmp_ne_u32_e32 vcc, 0, v2
	v_mov_b32_e32 v0, s6
	ds_read_b32 v0, v0
	s_cbranch_vccnz .LBB0_933
	v_readlane_b32 s8, v252, 0
	v_readlane_b32 s9, v252, 1
	s_load_dwordx2 s[6:7], s[8:9], 0x4
	s_mov_b32 s13, 1
	s_waitcnt lgkmcnt(0)
	s_mul_i32 s12, s6, s90
	s_mul_i32 s12, s12, s7
	s_branch .LBB0_920

; __device__ __forceinline__ unsigned xb_add(unsigned* p, unsigned v) { return __hip_atomic_fetch_add(p, v, __ATOMIC_RELAXED, __HIP_MEMORY_SCOPE_AGENT); }
; __device__ __forceinline__ bool xb_tid0(unsigned w0) { return w0 != 0u && __builtin_amdgcn_mbcnt_hi(0xffffffffu, __builtin_amdgcn_mbcnt_lo(0xffffffffu, 0u)) == 0u; }
; #define SEAM(k) do { if (IN((k) + 1)) xcd_barrier(bar); } while (0)
; __device__ __forceinline__ void xcd_barrier(const XcdBarrier& b) {
;     asm volatile("s_waitcnt vmcnt(0)" ::: "memory");
;     __syncthreads();
;     if (xb_tid0(b.w0)) {
;         unsigned* bar = b.bar;
;         __builtin_amdgcn_s_waitcnt(0);
;         unsigned nloc = b.st[0], nx = b.st[1];
;         if (nloc == 0u) { xcd_barrier_complete(bar, b.x, nloc, nx); b.st[0] = nloc; b.st[1] = nx; }
;         const unsigned old = xb_add(&bar[XB_XSUB(b.x)], 1u);
; __global__ void __launch_bounds__(512, 2) mk_fwd(Params P) {
;     ...
;             SEAM(pb + 9);
.LBB0_1530:
	v_readlane_b32 s4, v254, 54
	s_waitcnt vmcnt(0)
	s_add_i32 s22, s4, 10
	s_cmp_ge_i32 s22, s95
	s_cbranch_scc1 .LBB0_1543
	s_waitcnt vmcnt(0)
	v_readlane_b32 s28, v254, 35
	s_andn2_b64 vcc, exec, s[96:97]
	v_readlane_b32 s29, v254, 36
	v_mov_b64_e32 v[208:209], 0x29f
	s_waitcnt lgkmcnt(0)
	s_barrier
	s_cbranch_vccnz .LBB0_1586
	v_cmp_eq_u32_e32 vcc, 0, v226
	s_and_saveexec_b64 s[4:5], vcc
	s_cbranch_execz .LBB0_1585
	v_readlane_b32 s6, v253, 47
	s_waitcnt vmcnt(0) expcnt(0) lgkmcnt(0)
	buffer_inv sc1
	s_nop 0
	v_mov_b32_e32 v0, s6
	ds_read_b32 v2, v0
	v_readlane_b32 s6, v253, 48
	s_waitcnt lgkmcnt(0)
	v_cmp_ne_u32_e32 vcc, 0, v2
	v_mov_b32_e32 v0, s6
	ds_read_b32 v0, v0
	s_cbranch_vccnz .LBB0_1549
	v_readlane_b32 s8, v252, 0
	v_readlane_b32 s9, v252, 1
	s_load_dwordx2 s[6:7], s[8:9], 0x4
	s_mov_b32 s13, 1
	s_waitcnt lgkmcnt(0)
	s_mul_i32 s12, s6, s90
	s_mul_i32 s12, s12, s7
	s_branch .LBB0_1536

; __device__ __forceinline__ unsigned xb_add(unsigned* p, unsigned v) { return __hip_atomic_fetch_add(p, v, __ATOMIC_RELAXED, __HIP_MEMORY_SCOPE_AGENT); }
; __device__ __forceinline__ bool xb_tid0(unsigned w0) { return w0 != 0u && __builtin_amdgcn_mbcnt_hi(0xffffffffu, __builtin_amdgcn_mbcnt_lo(0xffffffffu, 0u)) == 0u; }
; __device__ __forceinline__ void xcd_barrier(const XcdBarrier& b) {
;     asm volatile("s_waitcnt vmcnt(0)" ::: "memory");
;     __syncthreads();
;     if (xb_tid0(b.w0)) {
;         unsigned* bar = b.bar;
;         __builtin_amdgcn_s_waitcnt(0);
;         unsigned nloc = b.st[0], nx = b.st[1];
;         if (nloc == 0u) { xcd_barrier_complete(bar, b.x, nloc, nx); b.st[0] = nloc; b.st[1] = nx; }
;         const unsigned old = xb_add(&bar[XB_XSUB(b.x)], 1u);
.LBB0_1616:
	v_readlane_b32 s6, v253, 47
	s_waitcnt vmcnt(0) expcnt(0) lgkmcnt(0)
	buffer_inv sc1
	s_nop 0
	v_mov_b32_e32 v0, s6
	ds_read_b32 v2, v0
	v_readlane_b32 s6, v253, 48
	s_waitcnt lgkmcnt(0)
	v_cmp_ne_u32_e32 vcc, 0, v2
	v_mov_b32_e32 v0, s6
	ds_read_b32 v0, v0
	s_cbranch_vccnz .LBB0_1631
	v_readlane_b32 s8, v252, 0
	v_readlane_b32 s9, v252, 1
	s_load_dwordx2 s[6:7], s[8:9], 0x4
	s_mov_b32 s13, 1
	s_waitcnt lgkmcnt(0)
	s_mul_i32 s12, s6, s90
	s_mul_i32 s12, s12, s7
	s_branch .LBB0_1619

; __device__ __forceinline__ unsigned xb_ld(unsigned* p)              { return __hip_atomic_load(p, __ATOMIC_RELAXED, __HIP_MEMORY_SCOPE_AGENT); }
; __device__ __forceinline__ unsigned xb_add(unsigned* p, unsigned v) { return __hip_atomic_fetch_add(p, v, __ATOMIC_RELAXED, __HIP_MEMORY_SCOPE_AGENT); }
; #define XB_SPIN(cond, bar) do { unsigned _sp = 0; while (cond) { __builtin_amdgcn_s_sleep(1); \
;     if ((++_sp & 255u) == 0u) { if (xb_ld(&(bar)[XB_TMO])) break; if (_sp > XB_SPIN_CAP) { atomicAdd(&(bar)[XB_TMO], 1u); break; } } } } while (0)
; __device__ __forceinline__ void xcd_barrier(const XcdBarrier& b) {
;     ...
;             if (og + 1u == (tg + 1u) * nx) xb_add(&bar[XB_TOPGEN], 1u);
;             else XB_SPIN(xb_ld(&bar[XB_TOPGEN]) == tg, bar);
;             __builtin_amdgcn_fence(__ATOMIC_ACQUIRE, "agent");
;             xb_add(&bar[XB_XGEN(b.x)], 1u);
;             asm volatile("s_waitcnt vmcnt(0)" ::: "memory");
.LBB0_1664:
	s_or_b64 exec, exec, s[6:7]
	s_mov_b64 s[6:7], exec
	v_mbcnt_lo_u32_b32 v0, s6, 0
	v_mbcnt_hi_u32_b32 v0, s7, v0
	v_cmp_eq_u32_e32 vcc, 0, v0
	s_waitcnt vmcnt(0)
	s_and_saveexec_b64 s[8:9], vcc
	s_cbranch_execnz .LBB0_1665
	s_getpc_b64 s[98:99]
